# PEER tables: the layer-0 rows of the down table also leave the prologue (all table conversion now runs on tile-less workgroups in the three layer-0 GEMM windows, rows re-split 27648 / 19968 / 17920)
# baseline (speedup 1.0000x reference)
.LBB0_34:
	s_andn2_b64 vcc, exec, s[22:23]
	s_cbranch_vccnz .LBB0_38
	s_add_i32 s48, s26, 0xffff5200
	s_and_b32 s49, s48, 0x7fff
	s_branch .LBB0_38
	s_cmpk_lt_u32 s48, 0x8000
	s_cselect_b64 s[22:23], -1, 0
	s_and_b64 s[24:25], s[22:23], exec
	s_cselect_b32 s25, s63, s65
	s_cselect_b32 s24, s62, s64
	s_lshl_b32 s50, s49, 13
	s_add_u32 s24, s24, s50
	s_addc_u32 s25, s25, 0
	v_lshl_add_u64 v[2:3], s[24:25], 0, v[36:37]
	global_load_dwordx4 v[30:33], v36, s[24:25] nt
	global_load_dwordx4 v[26:29], v36, s[24:25] offset:1024 nt
	global_load_dwordx4 v[22:25], v36, s[24:25] offset:2048 nt
	global_load_dwordx4 v[18:21], v36, s[24:25] offset:3072 nt
	v_add_co_u32_e32 v2, vcc, s42, v2
	v_and_b32_e32 v49, 64, v91
	s_nop 0
	v_addc_co_u32_e32 v3, vcc, 0, v3, vcc
	global_load_dwordx4 v[14:17], v[2:3], off nt
	global_load_dwordx4 v[10:13], v[2:3], off offset:1024 nt
	global_load_dwordx4 v[6:9], v[2:3], off offset:2048 nt
	s_nop 0
	global_load_dwordx4 v[2:5], v[2:3], off offset:3072 nt
	v_xor_b32_e32 v92, 1, v91
	v_add_u32_e32 v49, 64, v49
	v_cmp_lt_i32_e32 vcc, v92, v49
	s_waitcnt vmcnt(7)
	v_max_f32_e64 v93, |v33|, |v33|
	v_max_f32_e64 v94, |v32|, |v32|
	s_waitcnt vmcnt(6)
	v_max_f32_e64 v95, |v29|, |v29|
	v_max_f32_e64 v96, |v28|, |v28|
	s_waitcnt vmcnt(5)
	v_max_f32_e64 v97, |v25|, |v25|
	v_max_f32_e64 v98, |v24|, |v24|
	s_waitcnt vmcnt(4)
	v_max_f32_e64 v99, |v21|, |v21|
	v_max_f32_e64 v100, |v20|, |v20|
	v_max_f32_e32 v93, v94, v93
	v_max_f32_e32 v94, v96, v95
	v_max_f32_e32 v95, v98, v97
	v_max_f32_e32 v96, v100, v99
	v_max3_f32 v93, |v30|, |v31|, v93
	v_max3_f32 v94, |v26|, |v27|, v94
	s_waitcnt vmcnt(3)
	v_max_f32_e64 v97, |v17|, |v17|
	v_max_f32_e64 v98, |v16|, |v16|
	s_waitcnt vmcnt(2)
	v_max_f32_e64 v99, |v13|, |v13|
	v_max_f32_e64 v100, |v12|, |v12|
	v_max3_f32 v95, |v22|, |v23|, v95
	v_max3_f32 v96, |v18|, |v19|, v96
	s_waitcnt vmcnt(1)
	v_max_f32_e64 v101, |v9|, |v9|
	v_max_f32_e64 v102, |v8|, |v8|
	s_waitcnt vmcnt(0)
	v_max_f32_e64 v103, |v5|, |v5|
	v_max_f32_e64 v104, |v4|, |v4|
	v_max3_f32 v93, v93, 0, v94
	v_max_f32_e32 v94, v98, v97
	v_max_f32_e32 v97, v100, v99
	v_max_f32_e32 v98, v102, v101
	v_max_f32_e32 v99, v104, v103
	v_max3_f32 v93, v93, v95, v96
	v_max3_f32 v94, |v14|, |v15|, v94
	v_max3_f32 v95, |v10|, |v11|, v97
	v_cndmask_b32_e32 v92, v91, v92, vcc
	v_max3_f32 v96, |v6|, |v7|, v98
	v_max3_f32 v97, |v2|, |v3|, v99
	v_max3_f32 v93, v93, v94, v95
	v_lshlrev_b32_e32 v92, 2, v92
	v_max3_f32 v93, v93, v96, v97
	ds_bpermute_b32 v92, v92, v93
	v_xor_b32_e32 v94, 2, v91
	v_cmp_lt_i32_e32 vcc, v94, v49
	s_waitcnt lgkmcnt(0)
	v_max_f32_e32 v92, v92, v92
	v_cndmask_b32_e32 v94, v91, v94, vcc
	v_lshlrev_b32_e32 v94, 2, v94
	v_max_f32_e32 v92, v93, v92
	ds_bpermute_b32 v93, v94, v92
	v_xor_b32_e32 v94, 4, v91
	v_cmp_lt_i32_e32 vcc, v94, v49
	s_waitcnt lgkmcnt(0)
	v_max_f32_e32 v93, v93, v93
	v_cndmask_b32_e32 v94, v91, v94, vcc
	v_lshlrev_b32_e32 v94, 2, v94
	v_max_f32_e32 v92, v92, v93
	ds_bpermute_b32 v93, v94, v92
	v_xor_b32_e32 v94, 8, v91
	v_cmp_lt_i32_e32 vcc, v94, v49
	s_waitcnt lgkmcnt(0)
	v_max_f32_e32 v93, v93, v93
	v_cndmask_b32_e32 v94, v91, v94, vcc
	v_lshlrev_b32_e32 v94, 2, v94
	v_max_f32_e32 v92, v92, v93
	ds_bpermute_b32 v93, v94, v92
	v_xor_b32_e32 v94, 16, v91
	v_cmp_lt_i32_e32 vcc, v94, v49
	s_waitcnt lgkmcnt(0)
	v_max_f32_e32 v93, v93, v93
	v_cndmask_b32_e32 v94, v91, v94, vcc
	v_lshlrev_b32_e32 v94, 2, v94
	v_max_f32_e32 v92, v92, v93
	ds_bpermute_b32 v93, v94, v92
	v_xor_b32_e32 v94, 32, v91
	v_cmp_lt_i32_e32 vcc, v94, v49
	s_waitcnt lgkmcnt(0)
	v_max_f32_e32 v93, v93, v93
	v_cndmask_b32_e32 v49, v91, v94, vcc
	v_max_f32_e32 v92, v92, v93
	v_lshlrev_b32_e32 v49, 2, v49
	ds_bpermute_b32 v49, v49, v92
	s_waitcnt lgkmcnt(0)
	v_max_f32_e32 v49, v49, v49
	v_max_f32_e32 v49, v92, v49
	s_and_saveexec_b64 s[24:25], s[0:1]
	s_cbranch_execz .LBB0_37
	s_and_b64 s[50:51], s[22:23], exec
	s_mov_b32 s50, 0x12a00000
	s_cselect_b32 s50, s50, 0x12a20000
	s_add_u32 s50, s70, s50
	s_addc_u32 s51, s71, 0
	s_lshl_b32 s49, s49, 2
	v_mul_f32_e32 v92, 0x3b124925, v49
	v_mov_b32_e32 v93, s49
	global_store_dword v93, v92, s[50:51]

.LBB0_611:
	v_readlane_b32 s4, v255, 36
	v_readlane_b32 s8, v252, 0
	s_add_i32 s5, s4, 7
	v_readlane_b32 s9, v252, 1
	s_cmp_ge_i32 s5, s9
	v_readlane_b32 s10, v252, 2
	v_readlane_b32 s11, v252, 3
	s_cbranch_scc1 .LBB0_661
	v_readlane_b32 s4, v255, 34
	s_nop 0
	s_cmp_lg_u32 s4, 0
	s_cbranch_scc1 .Ldfa_done
	s_cmp_gt_u32 s82, 32
	s_cselect_b32 s11, 32, 0
	s_cmp_lt_u32 s2, s11
	s_cbranch_scc1 .Ldfa_done
	s_sub_u32 s10, s82, s11
	s_lshl_b32 s10, s10, 3
	s_sub_u32 s4, s2, s11
	s_lshl_b32 s4, s4, 3
	v_readfirstlane_b32 s11, v0
	s_lshr_b32 s11, s11, 6
	s_add_u32 s4, s4, s11
	s_add_u32 s4, s4, 0x0
	s_cmp_ge_u32 s4, 0x6c00
	s_cbranch_scc1 .Ldfa_done
	v_readlane_b32 s6, v252, 4
	v_readlane_b32 s7, v252, 5
	s_nop 0
	s_sub_u32 s6, s6, 0x38
	s_subb_u32 s7, s7, 0
	s_load_dwordx2 s[8:9], s[6:7], 0x0
	s_load_dwordx2 s[6:7], s[6:7], 0x20
	v_and_b32_e32 v6, 63, v0
	v_lshlrev_b32_e32 v7, 4, v6
	v_lshrrev_b32_e32 v56, 5, v6
	v_and_b32_e32 v57, 31, v6
	v_lshlrev_b32_e32 v56, 21, v56
	v_lshl_add_u32 v56, v57, 2, v56
	v_add_u32_e32 v56, 0xaa00000, v56
	s_mov_b64 exec, -1
	s_waitcnt lgkmcnt(0)
	s_lshl_b32 s11, s4, 13
	v_add_u32_e32 v40, s11, v7
	v_add_u32_e32 v41, 0x1000, v40
	global_load_dwordx4 v[8:11], v40, s[8:9] nt
	global_load_dwordx4 v[12:15], v40, s[8:9] offset:1024 nt
	global_load_dwordx4 v[16:19], v40, s[8:9] offset:2048 nt
	global_load_dwordx4 v[20:23], v40, s[8:9] offset:3072 nt
	global_load_dwordx4 v[24:27], v41, s[8:9] nt
	global_load_dwordx4 v[28:31], v41, s[8:9] offset:1024 nt
	global_load_dwordx4 v[32:35], v41, s[8:9] offset:2048 nt
	global_load_dwordx4 v[36:39], v41, s[8:9] offset:3072 nt
.Ldfa_loop:
	s_add_u32 s11, s4, s10
	s_min_u32 s11, s11, 0x6bff
	s_mov_b32 s101, s11
	s_lshl_b32 s11, s101, 13
	v_add_u32_e32 v40, s11, v7
	v_add_u32_e32 v41, 0x1000, v40
	global_load_dwordx4 v[76:79], v40, s[8:9] nt
	global_load_dwordx4 v[80:83], v40, s[8:9] offset:1024 nt
	global_load_dwordx4 v[84:87], v40, s[8:9] offset:2048 nt
	global_load_dwordx4 v[88:91], v40, s[8:9] offset:3072 nt
	global_load_dwordx4 v[92:95], v41, s[8:9] nt
	global_load_dwordx4 v[96:99], v41, s[8:9] offset:1024 nt
	global_load_dwordx4 v[100:103], v41, s[8:9] offset:2048 nt
	global_load_dwordx4 v[104:107], v41, s[8:9] offset:3072 nt
	s_waitcnt vmcnt(8)
	v_max3_f32 v42, |v8|, |v9|, |v10|
	v_max3_f32 v43, |v12|, |v13|, |v14|
	v_max3_f32 v44, |v16|, |v17|, |v18|
	v_max3_f32 v45, |v20|, |v21|, |v22|
	v_max3_f32 v46, |v24|, |v25|, |v26|
	v_max3_f32 v47, |v28|, |v29|, |v30|
	v_max3_f32 v48, |v32|, |v33|, |v34|
	v_max3_f32 v49, |v36|, |v37|, |v38|
	v_max_f32_e64 v42, v42, |v11|
	v_max_f32_e64 v43, v43, |v15|
	v_max_f32_e64 v44, v44, |v19|
	v_max_f32_e64 v45, v45, |v23|
	v_max_f32_e64 v46, v46, |v27|
	v_max_f32_e64 v47, v47, |v31|
	v_max_f32_e64 v48, v48, |v35|
	v_max_f32_e64 v49, v49, |v39|
	v_max3_f32 v42, v42, v43, v44
	v_max3_f32 v45, v45, v46, v47
	v_max3_f32 v42, v42, v45, v48
	v_max_f32_e32 v42, v42, v49
	s_nop 1
	v_max_f32_dpp v43, v42, v42 quad_perm:[1,0,3,2] row_mask:0xf bank_mask:0xf bound_ctrl:1
	s_nop 1
	v_max_f32_dpp v42, v43, v43 quad_perm:[2,3,0,1] row_mask:0xf bank_mask:0xf bound_ctrl:1
	s_nop 1
	v_max_f32_dpp v43, v42, v42 row_half_mirror row_mask:0xf bank_mask:0xf bound_ctrl:1
	s_nop 1
	v_max_f32_dpp v42, v43, v43 row_mirror row_mask:0xf bank_mask:0xf bound_ctrl:1
	s_nop 1
	v_mov_b32_e32 v43, v42
	s_nop 1
	v_permlane16_swap_b32_e32 v42, v43
	v_max_f32_e32 v42, v42, v43
	v_mov_b32_e32 v43, v42
	s_nop 1
	v_permlane32_swap_b32_e32 v42, v43
	v_max_f32_e32 v49, v42, v43
	v_mul_f32_e32 v44, 0x3b124925, v49
	s_lshl_b32 s11, s4, 2
	s_add_u32 s11, s11, 0x12a00000
	v_mov_b32_e32 v45, s11
	s_mov_b64 exec, 1
	global_store_dword v45, v44, s[6:7]
	s_mov_b64 exec, -1
	v_mov_b32_e32 v46, 0x43e00000
	v_div_scale_f32 v42, s[100:101], v49, v49, v46
	v_rcp_f32_e32 v43, v42
	s_nop 0
	v_fma_f32 v44, -v42, v43, 1.0
	v_fmac_f32_e32 v43, v44, v43
	v_div_scale_f32 v44, vcc, v46, v49, v46
	v_mul_f32_e32 v45, v44, v43
	v_fma_f32 v47, -v42, v45, v44
	v_fmac_f32_e32 v45, v47, v43
	v_fma_f32 v42, -v42, v45, v44
	s_nop 1
	v_div_fmas_f32 v42, v42, v43, v45
	v_div_fixup_f32 v42, v42, v49, v46
	v_cmp_lt_f32_e32 vcc, 0, v49
	s_nop 1
	v_cndmask_b32_e32 v48, 0, v42, vcc
	v_mul_f32_e32 v8, v8, v48
	v_mul_f32_e32 v9, v9, v48
	v_mul_f32_e32 v10, v10, v48
	v_mul_f32_e32 v11, v11, v48
	v_mul_f32_e32 v12, v12, v48
	v_mul_f32_e32 v13, v13, v48
	v_mul_f32_e32 v14, v14, v48
	v_mul_f32_e32 v15, v15, v48
	v_mul_f32_e32 v16, v16, v48
	v_mul_f32_e32 v17, v17, v48
	v_mul_f32_e32 v18, v18, v48
	v_mul_f32_e32 v19, v19, v48
	v_mul_f32_e32 v20, v20, v48
	v_mul_f32_e32 v21, v21, v48
	v_mul_f32_e32 v22, v22, v48
	v_mul_f32_e32 v23, v23, v48
	v_mul_f32_e32 v24, v24, v48
	v_mul_f32_e32 v25, v25, v48
	v_mul_f32_e32 v26, v26, v48
	v_mul_f32_e32 v27, v27, v48
	v_mul_f32_e32 v28, v28, v48
	v_mul_f32_e32 v29, v29, v48
	v_mul_f32_e32 v30, v30, v48
	v_mul_f32_e32 v31, v31, v48
	v_mul_f32_e32 v32, v32, v48
	v_mul_f32_e32 v33, v33, v48
	v_mul_f32_e32 v34, v34, v48
	v_mul_f32_e32 v35, v35, v48
	v_mul_f32_e32 v36, v36, v48
	v_mul_f32_e32 v37, v37, v48
	v_mul_f32_e32 v38, v38, v48
	v_mul_f32_e32 v39, v39, v48
	v_mov_b32_e32 v58, 0
	v_mov_b32_e32 v59, 0
	v_mov_b32_e32 v60, 0
	v_mov_b32_e32 v61, 0
	v_mov_b32_e32 v62, 0
	v_mov_b32_e32 v63, 0
	v_mov_b32_e32 v64, 0
	v_mov_b32_e32 v65, 0
	v_cvt_pk_fp8_f32 v58, v8, v9
	v_cvt_pk_fp8_f32 v59, v12, v13
	v_cvt_pk_fp8_f32 v60, v16, v17
	v_cvt_pk_fp8_f32 v61, v20, v21
	v_cvt_pk_fp8_f32 v62, v24, v25
	v_cvt_pk_fp8_f32 v63, v28, v29
	v_cvt_pk_fp8_f32 v64, v32, v33
	v_cvt_pk_fp8_f32 v65, v36, v37
	v_cvt_pk_fp8_f32 v58, v10, v11 op_sel:[0,0,1]
	v_cvt_pk_fp8_f32 v59, v14, v15 op_sel:[0,0,1]
	v_cvt_pk_fp8_f32 v60, v18, v19 op_sel:[0,0,1]
	v_cvt_pk_fp8_f32 v61, v22, v23 op_sel:[0,0,1]
	v_cvt_pk_fp8_f32 v62, v26, v27 op_sel:[0,0,1]
	v_cvt_pk_fp8_f32 v63, v30, v31 op_sel:[0,0,1]
	v_cvt_pk_fp8_f32 v64, v34, v35 op_sel:[0,0,1]
	v_cvt_pk_fp8_f32 v65, v38, v39 op_sel:[0,0,1]
	s_and_b32 s11, s4, 0x3fff
	s_lshl_b32 s11, s11, 7
	s_lshr_b32 s101, s4, 14
	s_lshl_b32 s101, s101, 25
	s_add_u32 s11, s11, s101
	v_add_u32_e32 v66, s11, v56
	v_add_u32_e32 v67, 0x400000, v66
	v_add_u32_e32 v68, 0x800000, v66
	v_add_u32_e32 v69, 0xc00000, v66
	v_add_u32_e32 v70, 0x1000000, v66
	v_add_u32_e32 v71, 0x1400000, v66
	v_add_u32_e32 v72, 0x1800000, v66
	v_add_u32_e32 v73, 0x1c00000, v66
	global_store_dword v66, v58, s[6:7] nt
	global_store_dword v67, v59, s[6:7] nt
	global_store_dword v68, v60, s[6:7] nt
	global_store_dword v69, v61, s[6:7] nt
	global_store_dword v70, v62, s[6:7] nt
	global_store_dword v71, v63, s[6:7] nt
	global_store_dword v72, v64, s[6:7] nt
	global_store_dword v73, v65, s[6:7] nt
	s_sleep 127
	s_add_u32 s4, s4, s10
	s_cmp_ge_u32 s4, 0x6c00
	s_cbranch_scc1 .Ldfa_done
	s_add_u32 s11, s4, s10
	s_min_u32 s11, s11, 0x6bff
	s_mov_b32 s101, s11
	s_lshl_b32 s11, s101, 13
	v_add_u32_e32 v40, s11, v7
	v_add_u32_e32 v41, 0x1000, v40
	global_load_dwordx4 v[8:11], v40, s[8:9] nt
	global_load_dwordx4 v[12:15], v40, s[8:9] offset:1024 nt
	global_load_dwordx4 v[16:19], v40, s[8:9] offset:2048 nt
	global_load_dwordx4 v[20:23], v40, s[8:9] offset:3072 nt
	global_load_dwordx4 v[24:27], v41, s[8:9] nt
	global_load_dwordx4 v[28:31], v41, s[8:9] offset:1024 nt
	global_load_dwordx4 v[32:35], v41, s[8:9] offset:2048 nt
	global_load_dwordx4 v[36:39], v41, s[8:9] offset:3072 nt
	s_waitcnt vmcnt(8)
	v_max3_f32 v42, |v76|, |v77|, |v78|
	v_max3_f32 v43, |v80|, |v81|, |v82|
	v_max3_f32 v44, |v84|, |v85|, |v86|
	v_max3_f32 v45, |v88|, |v89|, |v90|
	v_max3_f32 v46, |v92|, |v93|, |v94|
	v_max3_f32 v47, |v96|, |v97|, |v98|
	v_max3_f32 v48, |v100|, |v101|, |v102|
	v_max3_f32 v49, |v104|, |v105|, |v106|
	v_max_f32_e64 v42, v42, |v79|
	v_max_f32_e64 v43, v43, |v83|
	v_max_f32_e64 v44, v44, |v87|
	v_max_f32_e64 v45, v45, |v91|
	v_max_f32_e64 v46, v46, |v95|
	v_max_f32_e64 v47, v47, |v99|
	v_max_f32_e64 v48, v48, |v103|
	v_max_f32_e64 v49, v49, |v107|
	v_max3_f32 v42, v42, v43, v44
	v_max3_f32 v45, v45, v46, v47
	v_max3_f32 v42, v42, v45, v48
	v_max_f32_e32 v42, v42, v49
	s_nop 1
	v_max_f32_dpp v43, v42, v42 quad_perm:[1,0,3,2] row_mask:0xf bank_mask:0xf bound_ctrl:1
	s_nop 1
	v_max_f32_dpp v42, v43, v43 quad_perm:[2,3,0,1] row_mask:0xf bank_mask:0xf bound_ctrl:1
	s_nop 1
	v_max_f32_dpp v43, v42, v42 row_half_mirror row_mask:0xf bank_mask:0xf bound_ctrl:1
	s_nop 1
	v_max_f32_dpp v42, v43, v43 row_mirror row_mask:0xf bank_mask:0xf bound_ctrl:1
	s_nop 1
	v_mov_b32_e32 v43, v42
	s_nop 1
	v_permlane16_swap_b32_e32 v42, v43
	v_max_f32_e32 v42, v42, v43
	v_mov_b32_e32 v43, v42
	s_nop 1
	v_permlane32_swap_b32_e32 v42, v43
	v_max_f32_e32 v49, v42, v43
	v_mul_f32_e32 v44, 0x3b124925, v49
	s_lshl_b32 s11, s4, 2
	s_add_u32 s11, s11, 0x12a00000
	v_mov_b32_e32 v45, s11
	s_mov_b64 exec, 1
	global_store_dword v45, v44, s[6:7]
	s_mov_b64 exec, -1
	v_mov_b32_e32 v46, 0x43e00000
	v_div_scale_f32 v42, s[100:101], v49, v49, v46
	v_rcp_f32_e32 v43, v42
	s_nop 0
	v_fma_f32 v44, -v42, v43, 1.0
	v_fmac_f32_e32 v43, v44, v43
	v_div_scale_f32 v44, vcc, v46, v49, v46
	v_mul_f32_e32 v45, v44, v43
	v_fma_f32 v47, -v42, v45, v44
	v_fmac_f32_e32 v45, v47, v43
	v_fma_f32 v42, -v42, v45, v44
	s_nop 1
	v_div_fmas_f32 v42, v42, v43, v45
	v_div_fixup_f32 v42, v42, v49, v46
	v_cmp_lt_f32_e32 vcc, 0, v49
	s_nop 1
	v_cndmask_b32_e32 v48, 0, v42, vcc
	v_mul_f32_e32 v76, v76, v48
	v_mul_f32_e32 v77, v77, v48
	v_mul_f32_e32 v78, v78, v48
	v_mul_f32_e32 v79, v79, v48
	v_mul_f32_e32 v80, v80, v48
	v_mul_f32_e32 v81, v81, v48
	v_mul_f32_e32 v82, v82, v48
	v_mul_f32_e32 v83, v83, v48
	v_mul_f32_e32 v84, v84, v48
	v_mul_f32_e32 v85, v85, v48
	v_mul_f32_e32 v86, v86, v48
	v_mul_f32_e32 v87, v87, v48
	v_mul_f32_e32 v88, v88, v48
	v_mul_f32_e32 v89, v89, v48
	v_mul_f32_e32 v90, v90, v48
	v_mul_f32_e32 v91, v91, v48
	v_mul_f32_e32 v92, v92, v48
	v_mul_f32_e32 v93, v93, v48
	v_mul_f32_e32 v94, v94, v48
	v_mul_f32_e32 v95, v95, v48
	v_mul_f32_e32 v96, v96, v48
	v_mul_f32_e32 v97, v97, v48
	v_mul_f32_e32 v98, v98, v48
	v_mul_f32_e32 v99, v99, v48
	v_mul_f32_e32 v100, v100, v48
	v_mul_f32_e32 v101, v101, v48
	v_mul_f32_e32 v102, v102, v48
	v_mul_f32_e32 v103, v103, v48
	v_mul_f32_e32 v104, v104, v48
	v_mul_f32_e32 v105, v105, v48
	v_mul_f32_e32 v106, v106, v48
	v_mul_f32_e32 v107, v107, v48
	v_mov_b32_e32 v58, 0
	v_mov_b32_e32 v59, 0
	v_mov_b32_e32 v60, 0
	v_mov_b32_e32 v61, 0
	v_mov_b32_e32 v62, 0
	v_mov_b32_e32 v63, 0
	v_mov_b32_e32 v64, 0
	v_mov_b32_e32 v65, 0
	v_cvt_pk_fp8_f32 v58, v76, v77
	v_cvt_pk_fp8_f32 v59, v80, v81
	v_cvt_pk_fp8_f32 v60, v84, v85
	v_cvt_pk_fp8_f32 v61, v88, v89
	v_cvt_pk_fp8_f32 v62, v92, v93
	v_cvt_pk_fp8_f32 v63, v96, v97
	v_cvt_pk_fp8_f32 v64, v100, v101
	v_cvt_pk_fp8_f32 v65, v104, v105
	v_cvt_pk_fp8_f32 v58, v78, v79 op_sel:[0,0,1]
	v_cvt_pk_fp8_f32 v59, v82, v83 op_sel:[0,0,1]
	v_cvt_pk_fp8_f32 v60, v86, v87 op_sel:[0,0,1]
	v_cvt_pk_fp8_f32 v61, v90, v91 op_sel:[0,0,1]
	v_cvt_pk_fp8_f32 v62, v94, v95 op_sel:[0,0,1]
	v_cvt_pk_fp8_f32 v63, v98, v99 op_sel:[0,0,1]
	v_cvt_pk_fp8_f32 v64, v102, v103 op_sel:[0,0,1]
	v_cvt_pk_fp8_f32 v65, v106, v107 op_sel:[0,0,1]
	s_and_b32 s11, s4, 0x3fff
	s_lshl_b32 s11, s11, 7
	s_lshr_b32 s101, s4, 14
	s_lshl_b32 s101, s101, 25
	s_add_u32 s11, s11, s101
	v_add_u32_e32 v66, s11, v56
	v_add_u32_e32 v67, 0x400000, v66
	v_add_u32_e32 v68, 0x800000, v66
	v_add_u32_e32 v69, 0xc00000, v66
	v_add_u32_e32 v70, 0x1000000, v66
	v_add_u32_e32 v71, 0x1400000, v66
	v_add_u32_e32 v72, 0x1800000, v66
	v_add_u32_e32 v73, 0x1c00000, v66
	global_store_dword v66, v58, s[6:7] nt
	global_store_dword v67, v59, s[6:7] nt
	global_store_dword v68, v60, s[6:7] nt
	global_store_dword v69, v61, s[6:7] nt
	global_store_dword v70, v62, s[6:7] nt
	global_store_dword v71, v63, s[6:7] nt
	global_store_dword v72, v64, s[6:7] nt
	global_store_dword v73, v65, s[6:7] nt
	s_sleep 127
	s_add_u32 s4, s4, s10
	s_cmp_ge_u32 s4, 0x6c00
	s_cbranch_scc1 .Ldfa_done
	s_branch .Ldfa_loop

.LBB0_709:
	v_readlane_b32 s4, v255, 36
	v_readlane_b32 s8, v252, 0
	s_add_i32 s5, s4, 8
	v_readlane_b32 s9, v252, 1
	s_cmp_ge_i32 s5, s9
	v_readlane_b32 s10, v252, 2
	v_readlane_b32 s11, v252, 3
	s_cbranch_scc1 .LBB0_721
	v_readlane_b32 s4, v255, 34
	s_nop 0
	s_cmp_lg_u32 s4, 0
	s_cbranch_scc1 .Ldfb1_done
	s_cmp_gt_u32 s82, 32
	s_cselect_b32 s11, 32, 0
	s_cmp_lt_u32 s2, s11
	s_cbranch_scc1 .Ldfb1_done
	s_sub_u32 s10, s82, s11
	s_lshl_b32 s10, s10, 3
	s_sub_u32 s4, s2, s11
	s_lshl_b32 s4, s4, 3
	v_readfirstlane_b32 s11, v0
	s_lshr_b32 s11, s11, 6
	s_add_u32 s4, s4, s11
	s_add_u32 s4, s4, 0x6c00
	s_cmp_ge_u32 s4, 0x8000
	s_cbranch_scc1 .Ldfb1_done
	v_readlane_b32 s6, v252, 4
	v_readlane_b32 s7, v252, 5
	s_nop 0
	s_sub_u32 s6, s6, 0x38
	s_subb_u32 s7, s7, 0
	s_load_dwordx2 s[8:9], s[6:7], 0x0
	s_load_dwordx2 s[6:7], s[6:7], 0x20
	v_and_b32_e32 v6, 63, v0
	v_lshlrev_b32_e32 v7, 4, v6
	v_lshrrev_b32_e32 v56, 5, v6
	v_and_b32_e32 v57, 31, v6
	v_lshlrev_b32_e32 v56, 21, v56
	v_lshl_add_u32 v56, v57, 2, v56
	v_add_u32_e32 v56, 0xaa00000, v56
	s_mov_b64 exec, -1
	s_waitcnt lgkmcnt(0)
	s_lshl_b32 s11, s4, 13
	v_add_u32_e32 v40, s11, v7
	v_add_u32_e32 v41, 0x1000, v40
	global_load_dwordx4 v[8:11], v40, s[8:9] nt
	global_load_dwordx4 v[12:15], v40, s[8:9] offset:1024 nt
	global_load_dwordx4 v[16:19], v40, s[8:9] offset:2048 nt
	global_load_dwordx4 v[20:23], v40, s[8:9] offset:3072 nt
	global_load_dwordx4 v[24:27], v41, s[8:9] nt
	global_load_dwordx4 v[28:31], v41, s[8:9] offset:1024 nt
	global_load_dwordx4 v[32:35], v41, s[8:9] offset:2048 nt
	global_load_dwordx4 v[36:39], v41, s[8:9] offset:3072 nt

.Ldfb1_end:
	v_readlane_b32 s4, v255, 36
	v_readlane_b32 s4, v255, 34
	s_nop 0
	s_cmp_lg_u32 s4, 0
	s_cbranch_scc1 .Ldfb2_done
	s_cmp_gt_u32 s82, 32
	s_cselect_b32 s11, 32, 0
	s_cmp_lt_u32 s2, s11
	s_cbranch_scc1 .Ldfb2_done
	s_sub_u32 s10, s82, s11
	s_lshl_b32 s10, s10, 3
	s_sub_u32 s4, s2, s11
	s_lshl_b32 s4, s4, 3
	v_readfirstlane_b32 s11, v0
	s_lshr_b32 s11, s11, 6
	s_add_u32 s4, s4, s11
	s_add_u32 s4, s4, 0x0
	s_cmp_ge_u32 s4, 0x3a00
	s_cbranch_scc1 .Ldfb2_done
	v_readlane_b32 s6, v252, 4
	v_readlane_b32 s7, v252, 5
	s_nop 0
	s_sub_u32 s6, s6, 0x38
	s_subb_u32 s7, s7, 0
	s_load_dwordx2 s[8:9], s[6:7], 0x8
	s_load_dwordx2 s[6:7], s[6:7], 0x20
	v_and_b32_e32 v6, 63, v0
	v_lshlrev_b32_e32 v7, 4, v6
	v_lshrrev_b32_e32 v56, 5, v6
	v_and_b32_e32 v57, 31, v6
	v_lshlrev_b32_e32 v56, 21, v56
	v_lshl_add_u32 v56, v57, 2, v56
	v_add_u32_e32 v56, 0xea00000, v56
	s_mov_b64 exec, -1
	s_waitcnt lgkmcnt(0)
	s_lshl_b32 s11, s4, 13
	v_add_u32_e32 v40, s11, v7
	v_add_u32_e32 v41, 0x1000, v40
	global_load_dwordx4 v[8:11], v40, s[8:9] nt
	global_load_dwordx4 v[12:15], v40, s[8:9] offset:1024 nt
	global_load_dwordx4 v[16:19], v40, s[8:9] offset:2048 nt
	global_load_dwordx4 v[20:23], v40, s[8:9] offset:3072 nt
	global_load_dwordx4 v[24:27], v41, s[8:9] nt
	global_load_dwordx4 v[28:31], v41, s[8:9] offset:1024 nt
	global_load_dwordx4 v[32:35], v41, s[8:9] offset:2048 nt
	global_load_dwordx4 v[36:39], v41, s[8:9] offset:3072 nt
.Ldfb2_loop:
	s_add_u32 s11, s4, s10
	s_min_u32 s11, s11, 0x39ff
	s_mov_b32 s101, s11
	s_lshl_b32 s11, s101, 13
	v_add_u32_e32 v40, s11, v7
	v_add_u32_e32 v41, 0x1000, v40
	global_load_dwordx4 v[76:79], v40, s[8:9] nt
	global_load_dwordx4 v[80:83], v40, s[8:9] offset:1024 nt
	global_load_dwordx4 v[84:87], v40, s[8:9] offset:2048 nt
	global_load_dwordx4 v[88:91], v40, s[8:9] offset:3072 nt
	global_load_dwordx4 v[92:95], v41, s[8:9] nt
	global_load_dwordx4 v[96:99], v41, s[8:9] offset:1024 nt
	global_load_dwordx4 v[100:103], v41, s[8:9] offset:2048 nt
	global_load_dwordx4 v[104:107], v41, s[8:9] offset:3072 nt
	s_waitcnt vmcnt(8)
	v_max3_f32 v42, |v8|, |v9|, |v10|
	v_max3_f32 v43, |v12|, |v13|, |v14|
	v_max3_f32 v44, |v16|, |v17|, |v18|
	v_max3_f32 v45, |v20|, |v21|, |v22|
	v_max3_f32 v46, |v24|, |v25|, |v26|
	v_max3_f32 v47, |v28|, |v29|, |v30|
	v_max3_f32 v48, |v32|, |v33|, |v34|
	v_max3_f32 v49, |v36|, |v37|, |v38|
	v_max_f32_e64 v42, v42, |v11|
	v_max_f32_e64 v43, v43, |v15|
	v_max_f32_e64 v44, v44, |v19|
	v_max_f32_e64 v45, v45, |v23|
	v_max_f32_e64 v46, v46, |v27|
	v_max_f32_e64 v47, v47, |v31|
	v_max_f32_e64 v48, v48, |v35|
	v_max_f32_e64 v49, v49, |v39|
	v_max3_f32 v42, v42, v43, v44
	v_max3_f32 v45, v45, v46, v47
	v_max3_f32 v42, v42, v45, v48
	v_max_f32_e32 v42, v42, v49
	s_nop 1
	v_max_f32_dpp v43, v42, v42 quad_perm:[1,0,3,2] row_mask:0xf bank_mask:0xf bound_ctrl:1
	s_nop 1
	v_max_f32_dpp v42, v43, v43 quad_perm:[2,3,0,1] row_mask:0xf bank_mask:0xf bound_ctrl:1
	s_nop 1
	v_max_f32_dpp v43, v42, v42 row_half_mirror row_mask:0xf bank_mask:0xf bound_ctrl:1
	s_nop 1
	v_max_f32_dpp v42, v43, v43 row_mirror row_mask:0xf bank_mask:0xf bound_ctrl:1
	s_nop 1
	v_mov_b32_e32 v43, v42
	s_nop 1
	v_permlane16_swap_b32_e32 v42, v43
	v_max_f32_e32 v42, v42, v43
	v_mov_b32_e32 v43, v42
	s_nop 1
	v_permlane32_swap_b32_e32 v42, v43
	v_max_f32_e32 v49, v42, v43
	v_mul_f32_e32 v44, 0x3b124925, v49
	s_lshl_b32 s11, s4, 2
	s_add_u32 s11, s11, 0x12a20000
	v_mov_b32_e32 v45, s11
	s_mov_b64 exec, 1
	global_store_dword v45, v44, s[6:7]
	s_mov_b64 exec, -1
	v_mov_b32_e32 v46, 0x43e00000
	v_div_scale_f32 v42, s[100:101], v49, v49, v46
	v_rcp_f32_e32 v43, v42
	s_nop 0
	v_fma_f32 v44, -v42, v43, 1.0
	v_fmac_f32_e32 v43, v44, v43
	v_div_scale_f32 v44, vcc, v46, v49, v46
	v_mul_f32_e32 v45, v44, v43
	v_fma_f32 v47, -v42, v45, v44
	v_fmac_f32_e32 v45, v47, v43
	v_fma_f32 v42, -v42, v45, v44
	s_nop 1
	v_div_fmas_f32 v42, v42, v43, v45
	v_div_fixup_f32 v42, v42, v49, v46
	v_cmp_lt_f32_e32 vcc, 0, v49
	s_nop 1
	v_cndmask_b32_e32 v48, 0, v42, vcc
	v_mul_f32_e32 v8, v8, v48
	v_mul_f32_e32 v9, v9, v48
	v_mul_f32_e32 v10, v10, v48
	v_mul_f32_e32 v11, v11, v48
	v_mul_f32_e32 v12, v12, v48
	v_mul_f32_e32 v13, v13, v48
	v_mul_f32_e32 v14, v14, v48
	v_mul_f32_e32 v15, v15, v48
	v_mul_f32_e32 v16, v16, v48
	v_mul_f32_e32 v17, v17, v48
	v_mul_f32_e32 v18, v18, v48
	v_mul_f32_e32 v19, v19, v48
	v_mul_f32_e32 v20, v20, v48
	v_mul_f32_e32 v21, v21, v48
	v_mul_f32_e32 v22, v22, v48
	v_mul_f32_e32 v23, v23, v48
	v_mul_f32_e32 v24, v24, v48
	v_mul_f32_e32 v25, v25, v48
	v_mul_f32_e32 v26, v26, v48
	v_mul_f32_e32 v27, v27, v48
	v_mul_f32_e32 v28, v28, v48
	v_mul_f32_e32 v29, v29, v48
	v_mul_f32_e32 v30, v30, v48
	v_mul_f32_e32 v31, v31, v48
	v_mul_f32_e32 v32, v32, v48
	v_mul_f32_e32 v33, v33, v48
	v_mul_f32_e32 v34, v34, v48
	v_mul_f32_e32 v35, v35, v48
	v_mul_f32_e32 v36, v36, v48
	v_mul_f32_e32 v37, v37, v48
	v_mul_f32_e32 v38, v38, v48
	v_mul_f32_e32 v39, v39, v48
	v_mov_b32_e32 v58, 0
	v_mov_b32_e32 v59, 0
	v_mov_b32_e32 v60, 0
	v_mov_b32_e32 v61, 0
	v_mov_b32_e32 v62, 0
	v_mov_b32_e32 v63, 0
	v_mov_b32_e32 v64, 0
	v_mov_b32_e32 v65, 0
	v_cvt_pk_fp8_f32 v58, v8, v9
	v_cvt_pk_fp8_f32 v59, v12, v13
	v_cvt_pk_fp8_f32 v60, v16, v17
	v_cvt_pk_fp8_f32 v61, v20, v21
	v_cvt_pk_fp8_f32 v62, v24, v25
	v_cvt_pk_fp8_f32 v63, v28, v29
	v_cvt_pk_fp8_f32 v64, v32, v33
	v_cvt_pk_fp8_f32 v65, v36, v37
	v_cvt_pk_fp8_f32 v58, v10, v11 op_sel:[0,0,1]
	v_cvt_pk_fp8_f32 v59, v14, v15 op_sel:[0,0,1]
	v_cvt_pk_fp8_f32 v60, v18, v19 op_sel:[0,0,1]
	v_cvt_pk_fp8_f32 v61, v22, v23 op_sel:[0,0,1]
	v_cvt_pk_fp8_f32 v62, v26, v27 op_sel:[0,0,1]
	v_cvt_pk_fp8_f32 v63, v30, v31 op_sel:[0,0,1]
	v_cvt_pk_fp8_f32 v64, v34, v35 op_sel:[0,0,1]
	v_cvt_pk_fp8_f32 v65, v38, v39 op_sel:[0,0,1]
	s_and_b32 s11, s4, 0x3fff
	s_lshl_b32 s11, s11, 7
	s_lshr_b32 s101, s4, 14
	s_lshl_b32 s101, s101, 25
	s_add_u32 s11, s11, s101
	v_add_u32_e32 v66, s11, v56
	v_add_u32_e32 v67, 0x400000, v66
	v_add_u32_e32 v68, 0x800000, v66
	v_add_u32_e32 v69, 0xc00000, v66
	v_add_u32_e32 v70, 0x1000000, v66
	v_add_u32_e32 v71, 0x1400000, v66
	v_add_u32_e32 v72, 0x1800000, v66
	v_add_u32_e32 v73, 0x1c00000, v66
	global_store_dword v66, v58, s[6:7] nt
	global_store_dword v67, v59, s[6:7] nt
	global_store_dword v68, v60, s[6:7] nt
	global_store_dword v69, v61, s[6:7] nt
	global_store_dword v70, v62, s[6:7] nt
	global_store_dword v71, v63, s[6:7] nt
	global_store_dword v72, v64, s[6:7] nt
	global_store_dword v73, v65, s[6:7] nt
	s_sleep 127
	s_add_u32 s4, s4, s10
	s_cmp_ge_u32 s4, 0x3a00
	s_cbranch_scc1 .Ldfb2_done
	s_add_u32 s11, s4, s10
	s_min_u32 s11, s11, 0x39ff
	s_mov_b32 s101, s11
	s_lshl_b32 s11, s101, 13
	v_add_u32_e32 v40, s11, v7
	v_add_u32_e32 v41, 0x1000, v40
	global_load_dwordx4 v[8:11], v40, s[8:9] nt
	global_load_dwordx4 v[12:15], v40, s[8:9] offset:1024 nt
	global_load_dwordx4 v[16:19], v40, s[8:9] offset:2048 nt
	global_load_dwordx4 v[20:23], v40, s[8:9] offset:3072 nt
	global_load_dwordx4 v[24:27], v41, s[8:9] nt
	global_load_dwordx4 v[28:31], v41, s[8:9] offset:1024 nt
	global_load_dwordx4 v[32:35], v41, s[8:9] offset:2048 nt
	global_load_dwordx4 v[36:39], v41, s[8:9] offset:3072 nt
	s_waitcnt vmcnt(8)
	v_max3_f32 v42, |v76|, |v77|, |v78|
	v_max3_f32 v43, |v80|, |v81|, |v82|
	v_max3_f32 v44, |v84|, |v85|, |v86|
	v_max3_f32 v45, |v88|, |v89|, |v90|
	v_max3_f32 v46, |v92|, |v93|, |v94|
	v_max3_f32 v47, |v96|, |v97|, |v98|
	v_max3_f32 v48, |v100|, |v101|, |v102|
	v_max3_f32 v49, |v104|, |v105|, |v106|
	v_max_f32_e64 v42, v42, |v79|
	v_max_f32_e64 v43, v43, |v83|
	v_max_f32_e64 v44, v44, |v87|
	v_max_f32_e64 v45, v45, |v91|
	v_max_f32_e64 v46, v46, |v95|
	v_max_f32_e64 v47, v47, |v99|
	v_max_f32_e64 v48, v48, |v103|
	v_max_f32_e64 v49, v49, |v107|
	v_max3_f32 v42, v42, v43, v44
	v_max3_f32 v45, v45, v46, v47
	v_max3_f32 v42, v42, v45, v48
	v_max_f32_e32 v42, v42, v49
	s_nop 1
	v_max_f32_dpp v43, v42, v42 quad_perm:[1,0,3,2] row_mask:0xf bank_mask:0xf bound_ctrl:1
	s_nop 1
	v_max_f32_dpp v42, v43, v43 quad_perm:[2,3,0,1] row_mask:0xf bank_mask:0xf bound_ctrl:1
	s_nop 1
	v_max_f32_dpp v43, v42, v42 row_half_mirror row_mask:0xf bank_mask:0xf bound_ctrl:1
	s_nop 1
	v_max_f32_dpp v42, v43, v43 row_mirror row_mask:0xf bank_mask:0xf bound_ctrl:1
	s_nop 1
	v_mov_b32_e32 v43, v42
	s_nop 1
	v_permlane16_swap_b32_e32 v42, v43
	v_max_f32_e32 v42, v42, v43
	v_mov_b32_e32 v43, v42
	s_nop 1
	v_permlane32_swap_b32_e32 v42, v43
	v_max_f32_e32 v49, v42, v43
	v_mul_f32_e32 v44, 0x3b124925, v49
	s_lshl_b32 s11, s4, 2
	s_add_u32 s11, s11, 0x12a20000
	v_mov_b32_e32 v45, s11
	s_mov_b64 exec, 1
	global_store_dword v45, v44, s[6:7]
	s_mov_b64 exec, -1
	v_mov_b32_e32 v46, 0x43e00000
	v_div_scale_f32 v42, s[100:101], v49, v49, v46
	v_rcp_f32_e32 v43, v42
	s_nop 0
	v_fma_f32 v44, -v42, v43, 1.0
	v_fmac_f32_e32 v43, v44, v43
	v_div_scale_f32 v44, vcc, v46, v49, v46
	v_mul_f32_e32 v45, v44, v43
	v_fma_f32 v47, -v42, v45, v44
	v_fmac_f32_e32 v45, v47, v43
	v_fma_f32 v42, -v42, v45, v44
	s_nop 1
	v_div_fmas_f32 v42, v42, v43, v45
	v_div_fixup_f32 v42, v42, v49, v46
	v_cmp_lt_f32_e32 vcc, 0, v49
	s_nop 1
	v_cndmask_b32_e32 v48, 0, v42, vcc
	v_mul_f32_e32 v76, v76, v48
	v_mul_f32_e32 v77, v77, v48
	v_mul_f32_e32 v78, v78, v48
	v_mul_f32_e32 v79, v79, v48
	v_mul_f32_e32 v80, v80, v48
	v_mul_f32_e32 v81, v81, v48
	v_mul_f32_e32 v82, v82, v48
	v_mul_f32_e32 v83, v83, v48
	v_mul_f32_e32 v84, v84, v48
	v_mul_f32_e32 v85, v85, v48
	v_mul_f32_e32 v86, v86, v48
	v_mul_f32_e32 v87, v87, v48
	v_mul_f32_e32 v88, v88, v48
	v_mul_f32_e32 v89, v89, v48
	v_mul_f32_e32 v90, v90, v48
	v_mul_f32_e32 v91, v91, v48
	v_mul_f32_e32 v92, v92, v48
	v_mul_f32_e32 v93, v93, v48
	v_mul_f32_e32 v94, v94, v48
	v_mul_f32_e32 v95, v95, v48
	v_mul_f32_e32 v96, v96, v48
	v_mul_f32_e32 v97, v97, v48
	v_mul_f32_e32 v98, v98, v48
	v_mul_f32_e32 v99, v99, v48
	v_mul_f32_e32 v100, v100, v48
	v_mul_f32_e32 v101, v101, v48
	v_mul_f32_e32 v102, v102, v48
	v_mul_f32_e32 v103, v103, v48
	v_mul_f32_e32 v104, v104, v48
	v_mul_f32_e32 v105, v105, v48
	v_mul_f32_e32 v106, v106, v48
	v_mul_f32_e32 v107, v107, v48
	v_mov_b32_e32 v58, 0
	v_mov_b32_e32 v59, 0
	v_mov_b32_e32 v60, 0
	v_mov_b32_e32 v61, 0
	v_mov_b32_e32 v62, 0
	v_mov_b32_e32 v63, 0
	v_mov_b32_e32 v64, 0
	v_mov_b32_e32 v65, 0
	v_cvt_pk_fp8_f32 v58, v76, v77
	v_cvt_pk_fp8_f32 v59, v80, v81
	v_cvt_pk_fp8_f32 v60, v84, v85
	v_cvt_pk_fp8_f32 v61, v88, v89
	v_cvt_pk_fp8_f32 v62, v92, v93
	v_cvt_pk_fp8_f32 v63, v96, v97
	v_cvt_pk_fp8_f32 v64, v100, v101
	v_cvt_pk_fp8_f32 v65, v104, v105
	v_cvt_pk_fp8_f32 v58, v78, v79 op_sel:[0,0,1]
	v_cvt_pk_fp8_f32 v59, v82, v83 op_sel:[0,0,1]
	v_cvt_pk_fp8_f32 v60, v86, v87 op_sel:[0,0,1]
	v_cvt_pk_fp8_f32 v61, v90, v91 op_sel:[0,0,1]
	v_cvt_pk_fp8_f32 v62, v94, v95 op_sel:[0,0,1]
	v_cvt_pk_fp8_f32 v63, v98, v99 op_sel:[0,0,1]
	v_cvt_pk_fp8_f32 v64, v102, v103 op_sel:[0,0,1]
	v_cvt_pk_fp8_f32 v65, v106, v107 op_sel:[0,0,1]
	s_and_b32 s11, s4, 0x3fff
	s_lshl_b32 s11, s11, 7
	s_lshr_b32 s101, s4, 14
	s_lshl_b32 s101, s101, 25
	s_add_u32 s11, s11, s101
	v_add_u32_e32 v66, s11, v56
	v_add_u32_e32 v67, 0x400000, v66
	v_add_u32_e32 v68, 0x800000, v66
	v_add_u32_e32 v69, 0xc00000, v66
	v_add_u32_e32 v70, 0x1000000, v66
	v_add_u32_e32 v71, 0x1400000, v66
	v_add_u32_e32 v72, 0x1800000, v66
	v_add_u32_e32 v73, 0x1c00000, v66
	global_store_dword v66, v58, s[6:7] nt
	global_store_dword v67, v59, s[6:7] nt
	global_store_dword v68, v60, s[6:7] nt
	global_store_dword v69, v61, s[6:7] nt
	global_store_dword v70, v62, s[6:7] nt
	global_store_dword v71, v63, s[6:7] nt
	global_store_dword v72, v64, s[6:7] nt
	global_store_dword v73, v65, s[6:7] nt
	s_sleep 127
	s_add_u32 s4, s4, s10
	s_cmp_ge_u32 s4, 0x3a00
	s_cbranch_scc1 .Ldfb2_done
	s_branch .Ldfb2_loop

.LBB0_856:
	v_readlane_b32 s4, v255, 36
	v_readlane_b32 s8, v252, 0
	s_add_i32 s5, s4, 10
	v_readlane_b32 s9, v252, 1
	s_cmp_ge_i32 s5, s9
	v_readlane_b32 s10, v252, 2
	v_readlane_b32 s11, v252, 3
	s_cbranch_scc1 .LBB0_906
	v_readlane_b32 s4, v255, 34
	s_nop 0
	s_cmp_lg_u32 s4, 0
	s_cbranch_scc1 .Ldfc_done
	s_cmp_gt_u32 s82, 32
	s_cselect_b32 s11, 32, 0
	s_cmp_lt_u32 s2, s11
	s_cbranch_scc1 .Ldfc_done
	s_sub_u32 s10, s82, s11
	s_lshl_b32 s10, s10, 3
	s_sub_u32 s4, s2, s11
	s_lshl_b32 s4, s4, 3
	v_readfirstlane_b32 s11, v0
	s_lshr_b32 s11, s11, 6
	s_add_u32 s4, s4, s11
	s_add_u32 s4, s4, 0x3a00
	s_cmp_ge_u32 s4, 0x8000
	s_cbranch_scc1 .Ldfc_done
	v_readlane_b32 s6, v252, 4
	v_readlane_b32 s7, v252, 5
	s_nop 0
	s_sub_u32 s6, s6, 0x38
	s_subb_u32 s7, s7, 0
	s_load_dwordx2 s[8:9], s[6:7], 0x8
	s_load_dwordx2 s[6:7], s[6:7], 0x20
	v_and_b32_e32 v6, 63, v0
	v_lshlrev_b32_e32 v7, 4, v6
	v_lshrrev_b32_e32 v56, 5, v6
	v_and_b32_e32 v57, 31, v6
	v_lshlrev_b32_e32 v56, 21, v56
	v_lshl_add_u32 v56, v57, 2, v56
	v_add_u32_e32 v56, 0xea00000, v56
	s_mov_b64 exec, -1
	s_waitcnt lgkmcnt(0)
	s_lshl_b32 s11, s4, 13
	v_add_u32_e32 v40, s11, v7
	v_add_u32_e32 v41, 0x1000, v40
	global_load_dwordx4 v[8:11], v40, s[8:9] nt
	global_load_dwordx4 v[12:15], v40, s[8:9] offset:1024 nt
	global_load_dwordx4 v[16:19], v40, s[8:9] offset:2048 nt
	global_load_dwordx4 v[20:23], v40, s[8:9] offset:3072 nt
	global_load_dwordx4 v[24:27], v41, s[8:9] nt
	global_load_dwordx4 v[28:31], v41, s[8:9] offset:1024 nt
	global_load_dwordx4 v[32:35], v41, s[8:9] offset:2048 nt
	global_load_dwordx4 v[36:39], v41, s[8:9] offset:3072 nt
